# MoE GEMM1->GEMM2 hand-off: acquire invalidate removed (ACT rows are written once per phase with sc1 stores and never read before their ready flag)
# speedup vs baseline: 1.0031x; 1.0029x over previous
.LBB0_1048:
	global_load_dword v2, v1, s[8:9] sc1
	s_waitcnt vmcnt(0)
	v_readfirstlane_b32 s10, v2
	s_cmp_gt_u32 s10, 31
	s_mov_b64 s[10:11], -1
	s_cbranch_scc1 .LBB0_1047
	s_sleep 2
	global_load_dword v2, v1, s[8:9] sc1
	s_waitcnt vmcnt(0)
	v_readfirstlane_b32 s10, v2
	s_cmp_lt_u32 s10, 32
	s_mov_b64 s[10:11], -1
	s_cbranch_scc0 .LBB0_1047
	s_sleep 2
	global_load_dword v2, v1, s[8:9] sc1
	s_waitcnt vmcnt(0)
	v_readfirstlane_b32 s10, v2
	s_cmp_lt_u32 s10, 32
	s_mov_b64 s[10:11], -1
	s_cbranch_scc0 .LBB0_1047
	s_sleep 2
	global_load_dword v2, v1, s[8:9] sc1
	s_waitcnt vmcnt(0)
	v_readfirstlane_b32 s10, v2
	s_cmp_lt_u32 s10, 32
	s_mov_b64 s[10:11], -1
	s_cbranch_scc0 .LBB0_1047
	s_sleep 2
	global_load_dword v2, v1, s[8:9] sc1
	s_waitcnt vmcnt(0)
	v_readfirstlane_b32 s10, v2
	s_cmp_lt_u32 s10, 32
	s_mov_b64 s[10:11], -1
	s_cbranch_scc0 .LBB0_1047
	s_add_i32 s1, s1, -5
	s_cmp_eq_u32 s1, 0
	s_cselect_b64 s[10:11], -1, 0
	s_sleep 2
	s_branch .LBB0_1047
.LBB0_1054:
	s_waitcnt vmcnt(0)
.LBB0_1055:
	s_or_b64 exec, exec, s[6:7]
	v_and_b32_e32 v1, 15, v148
	v_and_b32_e32 v2, 0xf0, v131
	v_and_b32_e32 v3, 0x70, v130
	v_or_b32_e32 v2, v2, v1
	v_or_b32_e32 v3, v3, v1
	v_lshlrev_b32_e32 v1, 10, v2
	s_lshl_b32 s1, s68, 18
	v_add_u32_e32 v7, 0x20000, v1
	v_or_b32_e32 v8, s1, v154
	v_add_u32_e32 v2, s1, v7
	s_mul_hi_i32 s1, s69, 0x2aaaaaab
	s_lshr_b32 s6, s1, 31
	s_add_i32 s1, s1, s6
	s_barrier
	v_lshlrev_b32_e32 v156, 10, v3
	s_mul_i32 s10, s1, -6
	v_or_b32_e32 v6, 0x20000, v156
	s_add_i32 s10, s10, s69
	v_add_u32_e32 v155, 0x22800, v147
	v_or_b32_e32 v4, v8, v6
	v_or_b32_e32 v5, v2, v154
	v_or_b32_e32 v3, v8, v1
	v_or_b32_e32 v2, v8, v156
	s_cmp_lt_i32 s10, 2
	ds_write_b128 v155, v[2:5]
	s_cbranch_scc1 .LBB0_1061
	s_cmp_gt_i32 s10, 2
	s_cbranch_scc0 .LBB0_1062
	s_cmp_eq_u32 s10, 3
	s_mov_b64 s[6:7], -1
	s_cbranch_scc0 .LBB0_1059
	s_mov_b64 s[6:7], 0

.LBB0_1110:
	s_waitcnt lgkmcnt(0)
	s_waitcnt vmcnt(0)

.LBB0_2100:
	s_endpgm
.LBB0_2101:
	s_waitcnt vmcnt(0)
.LBB0_2102:
	s_or_b64 exec, exec, s[2:3]
	v_and_b32_e32 v0, 15, v2
	v_and_b32_e32 v1, 0xf0, v1
	v_or_b32_e32 v1, v1, v0
	v_and_b32_e32 v2, 0x70, v130
	v_lshlrev_b32_e32 v153, 10, v1
	s_lshl_b32 s2, s62, 18
	v_or_b32_e32 v0, v2, v0
	v_add_u32_e32 v5, 0x20000, v153
	s_mul_hi_i32 s6, s63, 0x2aaaaaab
	v_or_b32_e32 v6, s2, v152
	v_lshlrev_b32_e32 v154, 10, v0
	v_add_u32_e32 v0, s2, v5
	s_lshr_b32 s2, s6, 31
	s_add_i32 s6, s6, s2
	s_barrier
	s_mul_i32 s7, s6, -6
	v_or_b32_e32 v4, 0x20000, v154
	s_add_i32 s7, s7, s63
	v_add_u32_e32 v155, 0x22800, v143
	v_or_b32_e32 v2, v6, v4
	v_or_b32_e32 v3, v0, v152
	v_or_b32_e32 v1, v6, v153
	v_or_b32_e32 v0, v6, v154
	s_cmp_lt_i32 s7, 2
	ds_write_b128 v155, v[0:3]
	s_cbranch_scc1 .LBB0_2108
	s_cmp_gt_i32 s7, 2
	s_cbranch_scc0 .LBB0_2109
	s_cmp_eq_u32 s7, 3
	s_mov_b64 s[2:3], -1
	s_cbranch_scc0 .LBB0_2106
	s_mov_b64 s[2:3], 0

.LBB0_2157:
	s_waitcnt lgkmcnt(0)
	s_waitcnt vmcnt(0)
	s_mov_b32 s94, s36
